# P6 epilogue: staging-DMA wait moved behind the first copy's row/stats loads (in flight together)
# speedup vs baseline: 1.0007x; 1.0007x over previous
.LBB0_975:
	s_add_i32 s0, s96, s35
	s_ashr_i32 s1, s0, 31
	s_lshr_b32 s1, s1, 19
	s_add_i32 s0, s0, s1
	s_ashr_i32 s2, s0, 13
	s_xor_b64 s[14:15], s[6:7], -1
	s_ashr_i32 s0, s2, 31
	s_add_u32 s1, s2, s87
	s_addc_u32 s0, s0, 0
	s_waitcnt vmcnt(0)
	v_lshlrev_b32_e32 v186, 6, v179
	v_lshl_add_u32 v185, v179, 4, s85
	v_mov_b32_e32 v187, 0
	s_mul_i32 s40, s1, 0x6000
	s_add_u32 s40, s70, s40
	s_addc_u32 s41, s71, 0
	s_add_u32 s42, s40, 0x5000
	s_addc_u32 s43, s41, 0
	s_add_u32 s40, s40, 0x18000
	s_addc_u32 s41, s41, 0
	v_mov_b32_e32 v188, 0x10000
	v_lshl_add_u32 v188, v179, 4, v188
	s_add_i32 m0, s85, 0
	s_nop 0
	global_load_lds_dwordx4 v186, s[16:17] offset:0
	s_add_i32 m0, s85, 1008
	s_nop 0
	global_load_lds_dwordx4 v186, s[16:17] offset:16
	s_add_i32 m0, s85, 2016
	s_nop 0
	global_load_lds_dwordx4 v186, s[16:17] offset:32
	s_add_i32 m0, s85, 3024
	s_nop 0
	global_load_lds_dwordx4 v186, s[16:17] offset:48
	s_add_i32 m0, s85, 4096
	s_nop 0
	global_load_lds_dwordx4 v186, s[28:29] offset:0
	s_add_i32 m0, s85, 5104
	s_nop 0
	global_load_lds_dwordx4 v186, s[28:29] offset:16
	s_add_i32 m0, s85, 6112
	s_nop 0
	global_load_lds_dwordx4 v186, s[28:29] offset:32
	s_add_i32 m0, s85, 7120
	s_nop 0
	global_load_lds_dwordx4 v186, s[28:29] offset:48
	s_add_i32 m0, s85, 8192
	s_nop 0
	global_load_lds_dwordx4 v186, s[12:13] offset:0
	s_add_i32 m0, s85, 9200
	s_nop 0
	global_load_lds_dwordx4 v186, s[12:13] offset:16
	s_add_i32 m0, s85, 10208
	s_nop 0
	global_load_lds_dwordx4 v186, s[12:13] offset:32
	s_add_i32 m0, s85, 11216
	s_nop 0
	global_load_lds_dwordx4 v186, s[12:13] offset:48
	s_add_i32 m0, s85, 12288
	s_nop 0
	global_load_lds_dwordx4 v186, s[90:91] offset:0
	s_add_i32 m0, s85, 13296
	s_nop 0
	global_load_lds_dwordx4 v186, s[90:91] offset:16
	s_add_i32 m0, s85, 14304
	s_nop 0
	global_load_lds_dwordx4 v186, s[90:91] offset:32
	s_add_i32 m0, s85, 15312
	s_nop 0
	global_load_lds_dwordx4 v186, s[90:91] offset:48
	s_mov_b32 m0, 65536
	s_nop 0
	global_load_lds_dwordx4 v186, s[42:43] offset:0
	s_mov_b32 m0, 66544
	s_nop 0
	global_load_lds_dwordx4 v186, s[42:43] offset:16
	s_mov_b32 m0, 67552
	s_nop 0
	global_load_lds_dwordx4 v186, s[42:43] offset:32
	s_mov_b32 m0, 68560
	s_nop 0
	global_load_lds_dwordx4 v186, s[42:43] offset:48
	s_mov_b32 m0, 69632
	s_nop 0
	global_load_lds_dwordx4 v186, s[40:41] offset:0
	s_mov_b32 m0, 70640
	s_nop 0
	global_load_lds_dwordx4 v186, s[40:41] offset:16
	s_mov_b32 m0, 71648
	s_nop 0
	global_load_lds_dwordx4 v186, s[40:41] offset:32
	s_mov_b32 m0, 72656
	s_nop 0
	global_load_lds_dwordx4 v186, s[40:41] offset:48
	v_readlane_b32 s40, v253, 62
	v_readlane_b32 s41, v253, 63
	s_lshl_b64 s[44:45], s[96:97], 12
	v_lshlrev_b32_e32 v2, 6, v179
	s_add_u32 s40, s40, s44
	s_addc_u32 s41, s41, s45
	s_add_u32 s40, s40, 0x1000
	s_addc_u32 s41, s41, 0
	global_load_dword v184, v2, s[40:41]
	s_add_u32 s40, s40, 0x1000
	s_addc_u32 s41, s41, 0
	global_load_dword v184, v2, s[40:41]
	s_add_u32 s40, s40, 0x1000
	s_addc_u32 s41, s41, 0
	global_load_dword v184, v2, s[40:41]
	v_mov_b32_e32 v1, v179
	s_mulk_i32 s0, 0x6000
	s_mul_hi_u32 s3, s1, 0x6000
	s_add_i32 s3, s3, s0
	s_mulk_i32 s1, 0x6000
	v_lshlrev_b32_e32 v20, 4, v1
	s_add_u32 s6, s70, s1
	v_readlane_b32 s36, v253, 60
	v_ashrrev_i32_e32 v21, 31, v20
	s_addc_u32 s7, s71, s3
	s_lshl_b64 s[0:1], s[96:97], 12
	v_readlane_b32 s38, v253, 62
	v_lshlrev_b64 v[22:23], 2, v[20:21]
	v_readlane_b32 s39, v253, 63
	s_add_u32 s20, s38, s0
	v_lshl_add_u64 v[68:69], s[6:7], 0, v[22:23]
	s_mov_b64 s[6:7], 0x5000
	s_addc_u32 s21, s39, s1
	v_lshl_add_u64 v[12:13], v[68:69], 0, s[6:7]
	s_lshl_b64 s[6:7], s[96:97], 3
	v_lshl_add_u64 v[32:33], s[20:21], 0, v[22:23]
	s_add_u32 s6, s64, s6
	s_addc_u32 s7, s65, s7
	s_nop 0
	global_load_dwordx2 v[72:73], v3, s[6:7]
	global_load_dwordx4 v[16:19], v[32:33], off
	global_load_dwordx4 v[24:27], v[32:33], off offset:16
	global_load_dwordx4 v[28:31], v[32:33], off offset:32
	s_nop 0
	global_load_dwordx4 v[32:35], v[32:33], off offset:48
	s_waitcnt vmcnt(8)
	ds_read_b128 v[4:7], v188 offset:3072
	ds_read_b128 v[8:11], v188 offset:2048
	ds_read_b128 v[12:15], v188 offset:1024
	v_lshl_add_u64 v[60:61], s[16:17], 0, v[22:23]
	v_lshl_add_u64 v[64:65], s[28:29], 0, v[22:23]
	v_add_co_u32_e32 v68, vcc, s18, v68
	ds_read_b128 v[36:39], v185 offset:7168
	ds_read_b128 v[40:43], v185 offset:3072
	ds_read_b128 v[44:47], v185 offset:2048
	ds_read_b128 v[48:51], v185 offset:6144
	ds_read_b128 v[52:55], v185 offset:5120
	ds_read_b128 v[56:59], v185 offset:1024
	s_nop 0
	ds_read_b128 v[60:63], v185 offset:0
	s_nop 0
	ds_read_b128 v[64:67], v185 offset:4096
	v_addc_co_u32_e32 v69, vcc, 0, v69, vcc
	ds_read_b128 v[68:71], v188 offset:0
	v_add_u32_e32 v142, 64, v183
	v_xor_b32_e32 v1, 1, v178
	v_xor_b32_e32 v2, 2, v178
	v_cmp_lt_i32_e32 vcc, v1, v142
	v_xor_b32_e32 v74, 4, v178
	v_readlane_b32 s20, v255, 42
	v_cndmask_b32_e32 v1, v178, v1, vcc
	v_cmp_lt_i32_e32 vcc, v2, v142
	v_readlane_b32 s22, v255, 44
	s_add_u32 s0, s30, s0
	v_cndmask_b32_e32 v75, v178, v2, vcc
	v_lshlrev_b32_e32 v2, 2, v1
	v_lshlrev_b32_e32 v1, 2, v75
	v_cmp_lt_i32_e32 vcc, v74, v142
	s_addc_u32 s1, s31, s1
	v_readlane_b32 s37, v253, 61
	v_readlane_b32 s40, v254, 0
	v_readlane_b32 s41, v254, 1
	v_readlane_b32 s42, v254, 2
	v_readlane_b32 s43, v254, 3
	v_readlane_b32 s44, v254, 4
	v_readlane_b32 s45, v254, 5
	v_readlane_b32 s46, v254, 6
	v_readlane_b32 s47, v254, 7
	v_readlane_b32 s48, v254, 8
	v_readlane_b32 s49, v254, 9
	v_readlane_b32 s50, v254, 10
	v_readlane_b32 s51, v254, 11
	v_readlane_b32 s21, v255, 43
	v_readlane_b32 s23, v255, 45
	s_waitcnt lgkmcnt(0)
	s_waitcnt vmcnt(5)
	v_pk_add_f32 v[12:13], v[12:13], 1.0 op_sel_hi:[1,0]
	v_pk_add_f32 v[14:15], v[14:15], 1.0 op_sel_hi:[1,0]
	s_waitcnt lgkmcnt(0)
	s_waitcnt vmcnt(3)
	v_pk_add_f32 v[18:19], v[18:19], v[72:73] op_sel_hi:[1,0] neg_lo:[0,1] neg_hi:[0,1]
	v_pk_add_f32 v[4:5], v[4:5], 1.0 op_sel_hi:[1,0]
	v_pk_mul_f32 v[18:19], v[72:73], v[18:19] op_sel:[1,0]
	s_waitcnt lgkmcnt(0)
	s_waitcnt vmcnt(0)
	v_pk_add_f32 v[32:33], v[32:33], v[72:73] op_sel_hi:[1,0] neg_lo:[0,1] neg_hi:[0,1]
	v_pk_add_f32 v[34:35], v[34:35], v[72:73] op_sel_hi:[1,0] neg_lo:[0,1] neg_hi:[0,1]
	v_pk_mul_f32 v[32:33], v[72:73], v[32:33] op_sel:[1,0]
	v_pk_mul_f32 v[34:35], v[72:73], v[34:35] op_sel:[1,0]
	s_waitcnt lgkmcnt(0)
	s_waitcnt vmcnt(0)
	v_pk_fma_f32 v[32:33], v[32:33], v[40:41], v[36:37]
	v_pk_fma_f32 v[34:35], v[34:35], v[42:43], v[38:39]
	v_pk_mul_f32 v[32:33], v[32:33], s[34:35] op_sel_hi:[1,0]
	v_pk_add_f32 v[6:7], v[6:7], 1.0 op_sel_hi:[1,0]
	v_pk_add_f32 v[24:25], v[24:25], v[72:73] op_sel_hi:[1,0] neg_lo:[0,1] neg_hi:[0,1]
	v_pk_mul_f32 v[34:35], v[34:35], s[34:35] op_sel_hi:[1,0]
	v_pk_fma_f32 v[42:43], v[138:139], v[4:5], v[32:33]
	s_waitcnt lgkmcnt(0)
	s_waitcnt vmcnt(0)
	v_pk_fma_f32 v[4:5], v[18:19], v[62:63], v[66:67]
	v_pk_add_f32 v[16:17], v[16:17], v[72:73] op_sel_hi:[1,0] neg_lo:[0,1] neg_hi:[0,1]
	v_pk_mul_f32 v[24:25], v[72:73], v[24:25] op_sel:[1,0]
	v_pk_fma_f32 v[40:41], v[140:141], v[6:7], v[34:35]
	v_pk_mul_f32 v[4:5], v[4:5], s[34:35] op_sel_hi:[1,0]
	s_waitcnt lgkmcnt(0)
	s_waitcnt vmcnt(0)
	v_pk_add_f32 v[6:7], v[70:71], 1.0 op_sel_hi:[1,0]
	v_pk_fma_f32 v[24:25], v[24:25], v[56:57], v[52:53]
	v_pk_fma_f32 v[52:53], v[128:129], v[6:7], v[4:5]
	v_pk_mul_f32 v[4:5], v[72:73], v[16:17] op_sel:[1,0]
	v_pk_add_f32 v[26:27], v[26:27], v[72:73] op_sel_hi:[1,0] neg_lo:[0,1] neg_hi:[0,1]
	v_pk_fma_f32 v[4:5], v[60:61], v[4:5], v[64:65]
	v_pk_mul_f32 v[26:27], v[72:73], v[26:27] op_sel:[1,0]
	v_pk_mul_f32 v[4:5], v[4:5], s[34:35] op_sel_hi:[1,0]
	v_pk_add_f32 v[6:7], v[68:69], 1.0 op_sel_hi:[1,0]
	v_pk_fma_f32 v[26:27], v[26:27], v[58:59], v[54:55]
	v_pk_fma_f32 v[54:55], v[126:127], v[6:7], v[4:5]
	v_pk_add_f32 v[30:31], v[30:31], v[72:73] op_sel_hi:[1,0] neg_lo:[0,1] neg_hi:[0,1]
	v_add_f32_e32 v4, 0, v54
	v_add_f32_e32 v4, v4, v55
	v_pk_mul_f32 v[30:31], v[72:73], v[30:31] op_sel:[1,0]
	v_pk_mul_f32 v[24:25], v[24:25], s[34:35] op_sel_hi:[1,0]
	v_add_f32_e32 v4, v4, v52
	v_pk_add_f32 v[28:29], v[28:29], v[72:73] op_sel_hi:[1,0] neg_lo:[0,1] neg_hi:[0,1]
	v_pk_fma_f32 v[30:31], v[30:31], v[46:47], v[50:51]
	v_pk_fma_f32 v[50:51], v[130:131], v[12:13], v[24:25]
	v_add_f32_e32 v4, v4, v53
	v_pk_mul_f32 v[28:29], v[72:73], v[28:29] op_sel:[1,0]
	v_pk_mul_f32 v[26:27], v[26:27], s[34:35] op_sel_hi:[1,0]
	v_add_f32_e32 v4, v4, v50
	v_pk_fma_f32 v[28:29], v[28:29], v[44:45], v[48:49]
	v_pk_fma_f32 v[48:49], v[132:133], v[14:15], v[26:27]
	v_add_f32_e32 v4, v4, v51
	v_pk_add_f32 v[8:9], v[8:9], 1.0 op_sel_hi:[1,0]
	v_pk_mul_f32 v[28:29], v[28:29], s[34:35] op_sel_hi:[1,0]
	v_add_f32_e32 v4, v4, v48
	v_pk_fma_f32 v[46:47], v[134:135], v[8:9], v[28:29]
	v_add_f32_e32 v4, v4, v49
	v_pk_add_f32 v[10:11], v[10:11], 1.0 op_sel_hi:[1,0]
	v_pk_mul_f32 v[30:31], v[30:31], s[34:35] op_sel_hi:[1,0]
	v_add_f32_e32 v4, v4, v46
	v_pk_fma_f32 v[44:45], v[136:137], v[10:11], v[30:31]
	v_add_f32_e32 v4, v4, v47
	v_add_f32_e32 v4, v4, v44
	v_add_f32_e32 v4, v4, v45
	v_add_f32_e32 v4, v4, v42
	v_add_f32_e32 v4, v4, v43
	v_add_f32_e32 v4, v4, v40
	v_add_f32_e32 v4, v4, v41
	ds_bpermute_b32 v5, v2, v4
	v_cndmask_b32_e32 v6, v178, v74, vcc
	v_lshlrev_b32_e32 v74, 2, v6
	v_xor_b32_e32 v6, 8, v178
	v_cmp_lt_i32_e32 vcc, v6, v142
	s_waitcnt lgkmcnt(0)
	v_add_f32_e32 v4, v4, v5
	ds_bpermute_b32 v5, v1, v4
	v_cndmask_b32_e32 v6, v178, v6, vcc
	v_lshlrev_b32_e32 v75, 2, v6
	v_xor_b32_e32 v6, 16, v178
	v_cmp_lt_i32_e32 vcc, v6, v142
	s_waitcnt lgkmcnt(0)
	v_add_f32_e32 v4, v4, v5
	ds_bpermute_b32 v5, v74, v4
	v_cndmask_b32_e32 v6, v178, v6, vcc
	v_lshlrev_b32_e32 v126, 2, v6
	v_xor_b32_e32 v6, 32, v178
	v_cmp_lt_i32_e32 vcc, v6, v142
	s_waitcnt lgkmcnt(0)
	v_add_f32_e32 v7, v4, v5
	ds_bpermute_b32 v8, v75, v7
	v_cndmask_b32_e32 v4, v178, v6, vcc
	v_lshlrev_b32_e32 v127, 2, v4
	v_lshl_add_u64 v[4:5], s[12:13], 0, v[22:23]
	v_lshl_add_u64 v[36:37], s[90:91], 0, v[22:23]
	s_waitcnt lgkmcnt(0)
	v_add_f32_e32 v24, v7, v8
	ds_bpermute_b32 v25, v126, v24
	ds_read_b128 v[16:19], v185 offset:11264
	ds_read_b128 v[12:15], v185 offset:10240
	ds_read_b128 v[8:11], v185 offset:9216
	s_nop 0
	ds_read_b128 v[4:7], v185 offset:8192
	v_lshl_add_u64 v[22:23], s[0:1], 0, v[22:23]
	v_readlane_b32 s0, v255, 23
	v_readlane_b32 s1, v255, 24
	s_waitcnt lgkmcnt(0)
	v_add_f32_e32 v56, v24, v25
	ds_read_b128 v[24:27], v185 offset:15360
	ds_read_b128 v[28:31], v185 offset:14336
	ds_read_b128 v[32:35], v185 offset:13312
	s_nop 0
	ds_read_b128 v[36:39], v185 offset:12288
	ds_bpermute_b32 v57, v127, v56
	s_waitcnt lgkmcnt(0)
	v_add_f32_e32 v56, v56, v57
	v_mul_f32_e32 v56, 0x3a800000, v56
	v_pk_add_f32 v[54:55], v[54:55], v[56:57] op_sel_hi:[1,0] neg_lo:[0,1] neg_hi:[0,1]
	v_pk_add_f32 v[52:53], v[52:53], v[56:57] op_sel_hi:[1,0] neg_lo:[0,1] neg_hi:[0,1]
	v_pk_mul_f32 v[58:59], v[54:55], v[54:55]
	v_pk_mul_f32 v[60:61], v[52:53], v[52:53]
	v_add_f32_e32 v58, v58, v59
	v_pk_add_f32 v[50:51], v[50:51], v[56:57] op_sel_hi:[1,0] neg_lo:[0,1] neg_hi:[0,1]
	v_add_f32_e32 v58, v60, v58
	v_pk_mul_f32 v[62:63], v[50:51], v[50:51]
	v_add_f32_e32 v58, v61, v58
	v_pk_add_f32 v[48:49], v[48:49], v[56:57] op_sel_hi:[1,0] neg_lo:[0,1] neg_hi:[0,1]
	v_add_f32_e32 v58, v62, v58
	v_pk_mul_f32 v[64:65], v[48:49], v[48:49]
	v_add_f32_e32 v58, v63, v58
	v_pk_add_f32 v[46:47], v[46:47], v[56:57] op_sel_hi:[1,0] neg_lo:[0,1] neg_hi:[0,1]
	v_add_f32_e32 v58, v64, v58
	v_pk_mul_f32 v[66:67], v[46:47], v[46:47]
	v_add_f32_e32 v58, v65, v58
	v_pk_add_f32 v[44:45], v[44:45], v[56:57] op_sel_hi:[1,0] neg_lo:[0,1] neg_hi:[0,1]
	v_add_f32_e32 v58, v66, v58
	v_pk_mul_f32 v[68:69], v[44:45], v[44:45]
	v_add_f32_e32 v58, v67, v58
	v_pk_add_f32 v[42:43], v[42:43], v[56:57] op_sel_hi:[1,0] neg_lo:[0,1] neg_hi:[0,1]
	v_add_f32_e32 v58, v68, v58
	v_pk_mul_f32 v[70:71], v[42:43], v[42:43]
	v_add_f32_e32 v58, v69, v58
	v_pk_add_f32 v[40:41], v[40:41], v[56:57] op_sel_hi:[1,0] neg_lo:[0,1] neg_hi:[0,1]
	v_add_f32_e32 v58, v70, v58
	v_pk_mul_f32 v[56:57], v[40:41], v[40:41]
	v_add_f32_e32 v58, v71, v58
	v_add_f32_e32 v56, v56, v58
	v_add_f32_e32 v56, v57, v56
	ds_bpermute_b32 v57, v2, v56
	s_waitcnt lgkmcnt(0)
	v_add_f32_e32 v56, v56, v57
	ds_bpermute_b32 v57, v1, v56
	s_waitcnt lgkmcnt(0)
	v_add_f32_e32 v56, v56, v57
	ds_bpermute_b32 v57, v74, v56
	s_waitcnt lgkmcnt(0)
	v_add_f32_e32 v56, v56, v57
	ds_bpermute_b32 v57, v75, v56
	s_waitcnt lgkmcnt(0)
	v_add_f32_e32 v56, v56, v57
	ds_bpermute_b32 v57, v126, v56
	s_waitcnt lgkmcnt(0)
	v_add_f32_e32 v56, v56, v57
	ds_bpermute_b32 v57, v127, v56
	s_waitcnt lgkmcnt(0)
	v_add_f32_e32 v56, v56, v57
	v_fmamk_f32 v56, v56, 0x3a800000, v204
	v_mul_f32_e32 v57, 0x4b800000, v56
	v_cmp_gt_f32_e32 vcc, s22, v56
	s_nop 1
	v_cndmask_b32_e32 v56, v56, v57, vcc
	v_rsq_f32_e32 v56, v56
	s_nop 0
	v_mul_f32_e32 v57, 0x45800000, v56
	v_cndmask_b32_e32 v56, v56, v57, vcc
	v_pk_mul_f32 v[54:55], v[54:55], v[56:57] op_sel_hi:[1,0]
	v_pk_mul_f32 v[52:53], v[52:53], v[56:57] op_sel_hi:[1,0]
	s_waitcnt lgkmcnt(0)
	s_waitcnt vmcnt(0)
	v_pk_fma_f32 v[4:5], v[4:5], v[54:55], v[36:37]
	v_pk_mul_f32 v[36:37], v[50:51], v[56:57] op_sel_hi:[1,0]
	v_pk_fma_f32 v[6:7], v[6:7], v[52:53], v[38:39]
	v_pk_fma_f32 v[8:9], v[8:9], v[36:37], v[32:33]
	v_pk_mul_f32 v[32:33], v[48:49], v[56:57] op_sel_hi:[1,0]
	s_and_b64 vcc, exec, s[0:1]
	v_pk_fma_f32 v[10:11], v[10:11], v[32:33], v[34:35]
	v_pk_mul_f32 v[32:33], v[46:47], v[56:57] op_sel_hi:[1,0]
	s_nop 0
	v_pk_fma_f32 v[12:13], v[12:13], v[32:33], v[28:29]
	v_pk_mul_f32 v[28:29], v[44:45], v[56:57] op_sel_hi:[1,0]
	s_nop 0
	v_pk_fma_f32 v[14:15], v[14:15], v[28:29], v[30:31]
	v_pk_mul_f32 v[28:29], v[42:43], v[56:57] op_sel_hi:[1,0]
	s_nop 0
	v_pk_fma_f32 v[16:17], v[16:17], v[28:29], v[24:25]
	v_pk_mul_f32 v[24:25], v[40:41], v[56:57] op_sel_hi:[1,0]
	s_nop 0
	v_pk_fma_f32 v[18:19], v[18:19], v[24:25], v[26:27]
	global_store_dwordx4 v[22:23], v[4:7], off
	global_store_dwordx4 v[22:23], v[8:11], off offset:16
	global_store_dwordx4 v[22:23], v[12:15], off offset:32
	global_store_dwordx4 v[22:23], v[16:19], off offset:48
	s_cbranch_vccz .LBB0_977
	s_lshl_b64 s[0:1], s[96:97], 10
	s_mul_hi_i32 s3, s2, 0x6000
	s_mulk_i32 s2, 0x6000
	s_add_u32 s2, s70, s2
	s_addc_u32 s3, s71, s3
	v_lshl_add_u64 v[50:51], v[20:21], 2, s[2:3]
	s_mov_b64 s[2:3], 0x19000
	v_add_co_u32_e32 v34, vcc, s86, v50
	v_lshl_add_u64 v[30:31], v[50:51], 0, s[2:3]
	s_mov_b64 s[2:3], 0x18000
	v_addc_co_u32_e32 v35, vcc, 0, v51, vcc
	v_lshl_add_u64 v[46:47], v[50:51], 0, s[2:3]
	v_add_co_u32_e32 v50, vcc, s67, v50
	global_load_dwordx4 v[22:25], v[30:31], off offset:32
	global_load_dwordx4 v[26:29], v[30:31], off offset:16
	v_addc_co_u32_e32 v51, vcc, 0, v51, vcc
	global_load_dwordx4 v[30:33], v[30:31], off offset:48
	s_nop 0
	global_load_dwordx4 v[34:37], v[34:35], off
	s_nop 0
	ds_read_b128 v[38:41], v188 offset:5120
	ds_read_b128 v[42:45], v188 offset:7168
	s_nop 0
	ds_read_b128 v[46:49], v188 offset:6144
	s_lshl_b64 s[0:1], s[0:1], 1
	ds_read_b128 v[50:53], v188 offset:4096
	s_add_u32 s0, s76, s0
	s_addc_u32 s1, s77, s1
	v_lshl_add_u64 v[20:21], v[20:21], 1, s[0:1]
	s_waitcnt lgkmcnt(0)
	s_waitcnt vmcnt(3)
	v_pk_add_f32 v[22:23], v[22:23], 1.0 op_sel_hi:[1,0]
	s_waitcnt lgkmcnt(0)
	s_waitcnt vmcnt(2)
	v_pk_add_f32 v[26:27], v[26:27], 1.0 op_sel_hi:[1,0]
	v_pk_add_f32 v[28:29], v[28:29], 1.0 op_sel_hi:[1,0]
	s_waitcnt lgkmcnt(0)
	s_waitcnt vmcnt(0)
	v_pk_add_f32 v[34:35], v[34:35], 1.0 op_sel_hi:[1,0]
	v_pk_add_f32 v[36:37], v[36:37], 1.0 op_sel_hi:[1,0]
	v_pk_add_f32 v[24:25], v[24:25], 1.0 op_sel_hi:[1,0]
	v_pk_add_f32 v[30:31], v[30:31], 1.0 op_sel_hi:[1,0]
	v_pk_add_f32 v[32:33], v[32:33], 1.0 op_sel_hi:[1,0]
	s_waitcnt lgkmcnt(0)
	s_waitcnt vmcnt(0)
	v_pk_fma_f32 v[8:9], v[8:9], v[26:27], v[38:39]
	v_pk_fma_f32 v[10:11], v[10:11], v[28:29], v[40:41]
	s_waitcnt lgkmcnt(0)
	s_waitcnt vmcnt(0)
	v_pk_fma_f32 v[12:13], v[12:13], v[22:23], v[46:47]
	s_waitcnt lgkmcnt(0)
	s_waitcnt vmcnt(0)
	v_pk_fma_f32 v[4:5], v[4:5], v[34:35], v[50:51]
	v_pk_fma_f32 v[22:23], v[6:7], v[36:37], v[52:53]
	v_pk_fma_f32 v[14:15], v[14:15], v[24:25], v[48:49]
	v_pk_fma_f32 v[16:17], v[16:17], v[30:31], v[42:43]
	v_pk_fma_f32 v[18:19], v[18:19], v[32:33], v[44:45]
	v_cvt_pk_bf16_f32 v6, v8, v9
	v_cvt_pk_bf16_f32 v7, v10, v11
	v_cvt_pk_bf16_f32 v4, v4, v5
	v_cvt_pk_bf16_f32 v5, v22, v23
	v_cvt_pk_bf16_f32 v8, v12, v13
	v_cvt_pk_bf16_f32 v9, v14, v15
	v_cvt_pk_bf16_f32 v10, v16, v17
	v_cvt_pk_bf16_f32 v11, v18, v19
	global_store_dwordx4 v[20:21], v[4:7], off
	global_store_dwordx4 v[20:21], v[8:11], off offset:16
